# grid barrier: L1 invalidate issued at barrier entry (all waves parked, no loads until release) instead of after the release; plus c-load batching and parallel expert tile prefix
# speedup vs baseline: 1.0181x; 1.0181x over previous
.LBB0_10:
	global_load_dword v100, v[4:5], off
	global_load_dword v101, v[4:5], off offset:2048
	v_add_co_u32_e32 v108, vcc, 0x1000, v4
	s_nop 1
	v_addc_co_u32_e32 v109, vcc, 0, v5, vcc
	global_load_dword v102, v[108:109], off
	global_load_dword v103, v[108:109], off offset:2048
	v_add_co_u32_e32 v110, vcc, 0x2000, v4
	s_nop 1
	v_addc_co_u32_e32 v111, vcc, 0, v5, vcc
	global_load_dword v104, v[110:111], off
	global_load_dword v105, v[110:111], off offset:2048
	v_add_co_u32_e32 v112, vcc, 0x3000, v4
	s_nop 1
	v_addc_co_u32_e32 v113, vcc, 0, v5, vcc
	global_load_dword v106, v[112:113], off
	global_load_dword v107, v[112:113], off offset:2048
	s_waitcnt vmcnt(7)
	v_mul_f32_e32 v8, 0xbfb8aa3b, v100
	v_exp_f32_e32 v8, v8
	s_nop 0
	v_add_f32_e32 v8, 1.0, v8
	v_div_scale_f32 v9, s[22:23], v8, v8, v100
	v_rcp_f32_e32 v10, v9
	v_div_scale_f32 v11, vcc, v100, v8, v100
	v_fma_f32 v23, -v9, v10, 1.0
	v_fmac_f32_e32 v10, v23, v10
	v_mul_f32_e32 v23, v11, v10
	v_fma_f32 v24, -v9, v23, v11
	v_fmac_f32_e32 v23, v24, v10
	v_fma_f32 v9, -v9, v23, v11
	v_div_fmas_f32 v9, v9, v10, v23
	v_div_fixup_f32 v7, v9, v8, v100
	ds_write_b32 v2, v7
	s_waitcnt vmcnt(6)
	v_mul_f32_e32 v8, 0xbfb8aa3b, v101
	v_exp_f32_e32 v8, v8
	s_nop 0
	v_add_f32_e32 v8, 1.0, v8
	v_div_scale_f32 v9, s[22:23], v8, v8, v101
	v_rcp_f32_e32 v10, v9
	v_div_scale_f32 v11, vcc, v101, v8, v101
	v_fma_f32 v23, -v9, v10, 1.0
	v_fmac_f32_e32 v10, v23, v10
	v_mul_f32_e32 v23, v11, v10
	v_fma_f32 v24, -v9, v23, v11
	v_fmac_f32_e32 v23, v24, v10
	v_fma_f32 v9, -v9, v23, v11
	v_div_fmas_f32 v9, v9, v10, v23
	v_div_fixup_f32 v7, v9, v8, v101
	ds_write_b32 v2, v7 offset:2048
	s_waitcnt vmcnt(5)
	v_mul_f32_e32 v8, 0xbfb8aa3b, v102
	v_exp_f32_e32 v8, v8
	s_nop 0
	v_add_f32_e32 v8, 1.0, v8
	v_div_scale_f32 v9, s[22:23], v8, v8, v102
	v_rcp_f32_e32 v10, v9
	v_div_scale_f32 v11, vcc, v102, v8, v102
	v_fma_f32 v23, -v9, v10, 1.0
	v_fmac_f32_e32 v10, v23, v10
	v_mul_f32_e32 v23, v11, v10
	v_fma_f32 v24, -v9, v23, v11
	v_fmac_f32_e32 v23, v24, v10
	v_fma_f32 v9, -v9, v23, v11
	v_div_fmas_f32 v9, v9, v10, v23
	v_div_fixup_f32 v7, v9, v8, v102
	ds_write_b32 v2, v7 offset:4096
	s_waitcnt vmcnt(4)
	v_mul_f32_e32 v8, 0xbfb8aa3b, v103
	v_exp_f32_e32 v8, v8
	s_nop 0
	v_add_f32_e32 v8, 1.0, v8
	v_div_scale_f32 v9, s[22:23], v8, v8, v103
	v_rcp_f32_e32 v10, v9
	v_div_scale_f32 v11, vcc, v103, v8, v103
	v_fma_f32 v23, -v9, v10, 1.0
	v_fmac_f32_e32 v10, v23, v10
	v_mul_f32_e32 v23, v11, v10
	v_fma_f32 v24, -v9, v23, v11
	v_fmac_f32_e32 v23, v24, v10
	v_fma_f32 v9, -v9, v23, v11
	v_div_fmas_f32 v9, v9, v10, v23
	v_div_fixup_f32 v7, v9, v8, v103
	ds_write_b32 v2, v7 offset:6144
	s_waitcnt vmcnt(3)
	v_mul_f32_e32 v8, 0xbfb8aa3b, v104
	v_exp_f32_e32 v8, v8
	s_nop 0
	v_add_f32_e32 v8, 1.0, v8
	v_div_scale_f32 v9, s[22:23], v8, v8, v104
	v_rcp_f32_e32 v10, v9
	v_div_scale_f32 v11, vcc, v104, v8, v104
	v_fma_f32 v23, -v9, v10, 1.0
	v_fmac_f32_e32 v10, v23, v10
	v_mul_f32_e32 v23, v11, v10
	v_fma_f32 v24, -v9, v23, v11
	v_fmac_f32_e32 v23, v24, v10
	v_fma_f32 v9, -v9, v23, v11
	v_div_fmas_f32 v9, v9, v10, v23
	v_div_fixup_f32 v7, v9, v8, v104
	ds_write_b32 v2, v7 offset:8192
	s_waitcnt vmcnt(2)
	v_mul_f32_e32 v8, 0xbfb8aa3b, v105
	v_exp_f32_e32 v8, v8
	s_nop 0
	v_add_f32_e32 v8, 1.0, v8
	v_div_scale_f32 v9, s[22:23], v8, v8, v105
	v_rcp_f32_e32 v10, v9
	v_div_scale_f32 v11, vcc, v105, v8, v105
	v_fma_f32 v23, -v9, v10, 1.0
	v_fmac_f32_e32 v10, v23, v10
	v_mul_f32_e32 v23, v11, v10
	v_fma_f32 v24, -v9, v23, v11
	v_fmac_f32_e32 v23, v24, v10
	v_fma_f32 v9, -v9, v23, v11
	v_div_fmas_f32 v9, v9, v10, v23
	v_div_fixup_f32 v7, v9, v8, v105
	ds_write_b32 v2, v7 offset:10240
	s_waitcnt vmcnt(1)
	v_mul_f32_e32 v8, 0xbfb8aa3b, v106
	v_exp_f32_e32 v8, v8
	s_nop 0
	v_add_f32_e32 v8, 1.0, v8
	v_div_scale_f32 v9, s[22:23], v8, v8, v106
	v_rcp_f32_e32 v10, v9
	v_div_scale_f32 v11, vcc, v106, v8, v106
	v_fma_f32 v23, -v9, v10, 1.0
	v_fmac_f32_e32 v10, v23, v10
	v_mul_f32_e32 v23, v11, v10
	v_fma_f32 v24, -v9, v23, v11
	v_fmac_f32_e32 v23, v24, v10
	v_fma_f32 v9, -v9, v23, v11
	v_div_fmas_f32 v9, v9, v10, v23
	v_div_fixup_f32 v7, v9, v8, v106
	ds_write_b32 v2, v7 offset:12288
	s_waitcnt vmcnt(0)
	v_mul_f32_e32 v8, 0xbfb8aa3b, v107
	v_exp_f32_e32 v8, v8
	s_nop 0
	v_add_f32_e32 v8, 1.0, v8
	v_div_scale_f32 v9, s[22:23], v8, v8, v107
	v_rcp_f32_e32 v10, v9
	v_div_scale_f32 v11, vcc, v107, v8, v107
	v_fma_f32 v23, -v9, v10, 1.0
	v_fmac_f32_e32 v10, v23, v10
	v_mul_f32_e32 v23, v11, v10
	v_fma_f32 v24, -v9, v23, v11
	v_fmac_f32_e32 v23, v24, v10
	v_fma_f32 v9, -v9, v23, v11
	v_div_fmas_f32 v9, v9, v10, v23
	v_div_fixup_f32 v7, v9, v8, v107
	ds_write_b32 v2, v7 offset:14336
	s_or_b64 exec, exec, s[20:21]
	s_mul_i32 s20, s37, 48
	s_waitcnt lgkmcnt(0)
	s_barrier
	s_and_saveexec_b64 s[22:23], s[0:1]
	s_cbranch_execz .LBB0_19
	s_load_dwordx2 s[24:25], s[14:15], 0x10
	v_mov_b32_e32 v4, v3
	v_mov_b32_e32 v5, v3
	v_mov_b32_e32 v2, v3
	v_mov_b64_e32 v[10:11], v[4:5]
	v_ashrrev_i32_e32 v23, 31, v22
	v_mov_b64_e32 v[8:9], v[2:3]
	v_mov_b64_e32 v[6:7], v[4:5]
	v_lshlrev_b64 v[28:29], 2, v[22:23]
	v_mov_b32_e32 v26, v1
	v_mov_b64_e32 v[4:5], v[2:3]
	v_mov_b32_e32 v2, v31
	s_and_saveexec_b64 s[26:27], s[6:7]
	s_cbranch_execz .LBB0_16
	s_waitcnt lgkmcnt(0)
	v_lshl_add_u64 v[4:5], s[24:25], 0, v[20:21]
	v_lshl_add_u64 v[24:25], v[4:5], 0, v[28:29]
	v_mov_b32_e32 v4, 0
	s_mov_b64 s[28:29], 0
	v_mov_b32_e32 v2, v13
	v_mov_b32_e32 v23, v32
	v_mov_b32_e32 v26, v1
	v_mov_b32_e32 v5, v4
	v_mov_b32_e32 v6, v4
	v_mov_b32_e32 v7, v4
	v_mov_b32_e32 v8, v4
	v_mov_b32_e32 v9, v4
	v_mov_b32_e32 v10, v4
	v_mov_b32_e32 v11, v4

.LBB0_104:
	s_load_dwordx4 s[0:3], s[96:97], 0xb8
	s_waitcnt lgkmcnt(0)
	s_mov_b64 s[6:7], s[2:3]
	s_cmp_lt_i32 s6, 2
	s_mov_b64 s[4:5], s[0:1]
	s_cselect_b64 s[2:3], -1, 0
	s_cmp_gt_i32 s7, 2
	s_cselect_b64 s[0:1], -1, 0
	s_and_b64 s[2:3], s[2:3], s[0:1]
	s_andn2_b64 vcc, exec, s[2:3]
	s_cbranch_vccnz .LBB0_158
	s_waitcnt vmcnt(0)
	s_barrier
	s_mov_b64 s[2:3], exec
	v_readlane_b32 s4, v243, 10
	v_readlane_b32 s5, v243, 11
	s_and_b64 s[4:5], s[2:3], s[4:5]
	s_mov_b64 exec, s[4:5]
	s_cbranch_execz .LBB0_157
	s_add_i32 s4, 0, 0x20000
	v_mov_b32_e32 v1, s4
	s_waitcnt vmcnt(0) expcnt(0) lgkmcnt(0)
	buffer_inv sc1
	ds_read_b32 v3, v1
	s_add_i32 s4, 0, 0x20004
	v_mov_b32_e32 v1, s4
	ds_read_b32 v1, v1
	s_waitcnt lgkmcnt(1)
	v_cmp_ne_u32_e32 vcc, 0, v3
	s_cbranch_vccnz .LBB0_121
	v_readlane_b32 s4, v243, 4
	v_readlane_b32 s5, v243, 5
	s_load_dwordx2 s[8:9], s[4:5], 0x4
	s_load_dwordx4 s[40:43], s[96:97], 0xb8
	s_mov_b32 s47, 1
	v_mov_b32_e32 v17, 0
	s_waitcnt lgkmcnt(0)
	s_mul_i32 s46, s8, s33
	s_add_u32 s4, s40, 0x4200
	s_addc_u32 s5, s41, 0
	s_add_u32 s6, s40, 0x4400
	s_addc_u32 s7, s41, 0
	s_add_u32 s8, s40, 0x4500
	s_mul_i32 s46, s46, s9
	s_addc_u32 s9, s41, 0
	s_add_u32 s10, s40, 0x4600
	s_addc_u32 s11, s41, 0
	s_add_u32 s12, s40, 0x4700
	s_addc_u32 s13, s41, 0
	s_add_u32 s14, s40, 0x4800
	s_addc_u32 s15, s41, 0
	s_add_u32 s16, s40, 0x4900
	s_addc_u32 s17, s41, 0
	s_add_u32 s18, s40, 0x4a00
	s_addc_u32 s19, s41, 0
	s_add_u32 s20, s40, 0x4b00
	s_addc_u32 s21, s41, 0
	s_add_u32 s22, s40, 0x4c00
	s_addc_u32 s23, s41, 0
	s_add_u32 s24, s40, 0x4d00
	s_addc_u32 s25, s41, 0
	s_add_u32 s26, s40, 0x4e00
	s_addc_u32 s27, s41, 0
	s_add_u32 s28, s40, 0x4f00
	s_addc_u32 s29, s41, 0
	s_add_u32 s30, s40, 0x5000
	s_addc_u32 s31, s41, 0
	s_add_u32 s34, s40, 0x5100
	s_addc_u32 s35, s41, 0
	s_add_u32 s36, s40, 0x5200
	s_addc_u32 s37, s41, 0
	s_add_u32 s38, s40, 0x5300
	s_addc_u32 s39, s41, 0
	s_branch .LBB0_109

.LBB0_136:
	s_or_b64 exec, exec, s[8:9]
	s_waitcnt vmcnt(0)
	s_waitcnt vmcnt(0)

.LBB0_154:
	s_or_b64 exec, exec, s[6:7]
	s_mov_b64 s[6:7], exec
	v_mbcnt_lo_u32_b32 v1, s6, 0
	v_mbcnt_hi_u32_b32 v1, s7, v1
	v_cmp_eq_u32_e32 vcc, 0, v1
	s_waitcnt vmcnt(0)
	s_and_saveexec_b64 s[8:9], vcc
	s_cbranch_execz .LBB0_156
	s_bcnt1_i32_b64 s6, s[6:7]
	v_mov_b32_e32 v1, 0x2000
	v_mov_b32_e32 v2, s6
	global_atomic_add v1, v2, s[4:5] offset:1024

.LBB0_327:
	s_load_dwordx4 s[0:3], s[96:97], 0xb8
	s_waitcnt lgkmcnt(0)
	s_mov_b64 s[6:7], s[2:3]
	s_cmp_lt_i32 s6, 4
	s_mov_b64 s[4:5], s[0:1]
	s_cselect_b64 s[2:3], -1, 0
	s_cmp_gt_i32 s7, 4
	s_cselect_b64 s[0:1], -1, 0
	s_and_b64 s[2:3], s[2:3], s[0:1]
	s_andn2_b64 vcc, exec, s[2:3]
	s_cbranch_vccnz .LBB0_381
	s_waitcnt vmcnt(0)
	s_barrier
	s_mov_b64 s[2:3], exec
	v_readlane_b32 s4, v243, 10
	v_readlane_b32 s5, v243, 11
	s_and_b64 s[4:5], s[2:3], s[4:5]
	s_mov_b64 exec, s[4:5]
	s_cbranch_execz .LBB0_380
	s_add_i32 s4, 0, 0x20000
	v_mov_b32_e32 v1, s4
	s_waitcnt vmcnt(0) expcnt(0) lgkmcnt(0)
	buffer_inv sc1
	ds_read_b32 v3, v1
	s_add_i32 s4, 0, 0x20004
	v_mov_b32_e32 v1, s4
	ds_read_b32 v1, v1
	s_waitcnt lgkmcnt(1)
	v_cmp_ne_u32_e32 vcc, 0, v3
	s_cbranch_vccnz .LBB0_344
	v_readlane_b32 s4, v243, 4
	v_readlane_b32 s5, v243, 5
	s_load_dwordx2 s[8:9], s[4:5], 0x4
	s_load_dwordx4 s[40:43], s[96:97], 0xb8
	s_mov_b32 s47, 1
	v_mov_b32_e32 v17, 0
	s_waitcnt lgkmcnt(0)
	s_mul_i32 s46, s8, s33
	s_add_u32 s4, s40, 0x4200
	s_addc_u32 s5, s41, 0
	s_add_u32 s6, s40, 0x4400
	s_addc_u32 s7, s41, 0
	s_add_u32 s8, s40, 0x4500
	s_mul_i32 s46, s46, s9
	s_addc_u32 s9, s41, 0
	s_add_u32 s10, s40, 0x4600
	s_addc_u32 s11, s41, 0
	s_add_u32 s12, s40, 0x4700
	s_addc_u32 s13, s41, 0
	s_add_u32 s14, s40, 0x4800
	s_addc_u32 s15, s41, 0
	s_add_u32 s16, s40, 0x4900
	s_addc_u32 s17, s41, 0
	s_add_u32 s18, s40, 0x4a00
	s_addc_u32 s19, s41, 0
	s_add_u32 s20, s40, 0x4b00
	s_addc_u32 s21, s41, 0
	s_add_u32 s22, s40, 0x4c00
	s_addc_u32 s23, s41, 0
	s_add_u32 s24, s40, 0x4d00
	s_addc_u32 s25, s41, 0
	s_add_u32 s26, s40, 0x4e00
	s_addc_u32 s27, s41, 0
	s_add_u32 s28, s40, 0x4f00
	s_addc_u32 s29, s41, 0
	s_add_u32 s30, s40, 0x5000
	s_addc_u32 s31, s41, 0
	s_add_u32 s34, s40, 0x5100
	s_addc_u32 s35, s41, 0
	s_add_u32 s36, s40, 0x5200
	s_addc_u32 s37, s41, 0
	s_add_u32 s38, s40, 0x5300
	s_addc_u32 s39, s41, 0
	s_branch .LBB0_332

.LBB0_542:
	s_load_dwordx4 s[4:7], s[96:97], 0xb8
	s_waitcnt lgkmcnt(0)
	s_cmp_gt_i32 s7, 5
	s_cselect_b64 s[0:1], -1, 0
	s_and_b64 s[2:3], s[2:3], s[0:1]
	s_andn2_b64 vcc, exec, s[2:3]
	s_cbranch_vccnz .LBB0_596
	s_waitcnt vmcnt(0)
	s_barrier
	s_mov_b64 s[2:3], exec
	v_readlane_b32 s4, v243, 10
	v_readlane_b32 s5, v243, 11
	s_and_b64 s[4:5], s[2:3], s[4:5]
	s_mov_b64 exec, s[4:5]
	s_cbranch_execz .LBB0_595
	s_add_i32 s4, 0, 0x20000
	v_mov_b32_e32 v1, s4
	s_waitcnt vmcnt(0) expcnt(0) lgkmcnt(0)
	buffer_inv sc1
	ds_read_b32 v3, v1
	s_add_i32 s4, 0, 0x20004
	v_mov_b32_e32 v1, s4
	ds_read_b32 v1, v1
	s_waitcnt lgkmcnt(1)
	v_cmp_ne_u32_e32 vcc, 0, v3
	s_cbranch_vccnz .LBB0_559
	v_readlane_b32 s4, v243, 4
	v_readlane_b32 s5, v243, 5
	s_load_dwordx2 s[8:9], s[4:5], 0x4
	s_load_dwordx4 s[40:43], s[96:97], 0xb8
	s_mov_b32 s47, 1
	v_mov_b32_e32 v17, 0
	s_waitcnt lgkmcnt(0)
	s_mul_i32 s46, s8, s33
	s_add_u32 s4, s40, 0x4200
	s_addc_u32 s5, s41, 0
	s_add_u32 s6, s40, 0x4400
	s_addc_u32 s7, s41, 0
	s_add_u32 s8, s40, 0x4500
	s_mul_i32 s46, s46, s9
	s_addc_u32 s9, s41, 0
	s_add_u32 s10, s40, 0x4600
	s_addc_u32 s11, s41, 0
	s_add_u32 s12, s40, 0x4700
	s_addc_u32 s13, s41, 0
	s_add_u32 s14, s40, 0x4800
	s_addc_u32 s15, s41, 0
	s_add_u32 s16, s40, 0x4900
	s_addc_u32 s17, s41, 0
	s_add_u32 s18, s40, 0x4a00
	s_addc_u32 s19, s41, 0
	s_add_u32 s20, s40, 0x4b00
	s_addc_u32 s21, s41, 0
	s_add_u32 s22, s40, 0x4c00
	s_addc_u32 s23, s41, 0
	s_add_u32 s24, s40, 0x4d00
	s_addc_u32 s25, s41, 0
	s_add_u32 s26, s40, 0x4e00
	s_addc_u32 s27, s41, 0
	s_add_u32 s28, s40, 0x4f00
	s_addc_u32 s29, s41, 0
	s_add_u32 s30, s40, 0x5000
	s_addc_u32 s31, s41, 0
	s_add_u32 s34, s40, 0x5100
	s_addc_u32 s35, s41, 0
	s_add_u32 s36, s40, 0x5200
	s_addc_u32 s37, s41, 0
	s_add_u32 s38, s40, 0x5300
	s_addc_u32 s39, s41, 0
	s_branch .LBB0_547

.LBB0_600:
	s_load_dwordx4 s[4:7], s[96:97], 0xb8
	s_waitcnt lgkmcnt(0)
	s_cmp_gt_i32 s7, 6
	s_cselect_b64 s[0:1], -1, 0
	s_and_b64 s[2:3], s[2:3], s[0:1]
	s_andn2_b64 vcc, exec, s[2:3]
	s_cbranch_vccnz .LBB0_654
	s_waitcnt vmcnt(0)
	s_barrier
	s_mov_b64 s[2:3], exec
	v_readlane_b32 s4, v243, 10
	v_readlane_b32 s5, v243, 11
	s_and_b64 s[4:5], s[2:3], s[4:5]
	s_mov_b64 exec, s[4:5]
	s_cbranch_execz .LBB0_653
	s_add_i32 s4, 0, 0x20000
	v_mov_b32_e32 v1, s4
	s_waitcnt vmcnt(0) expcnt(0) lgkmcnt(0)
	buffer_inv sc1
	ds_read_b32 v3, v1
	s_add_i32 s4, 0, 0x20004
	v_mov_b32_e32 v1, s4
	ds_read_b32 v1, v1
	s_waitcnt lgkmcnt(1)
	v_cmp_ne_u32_e32 vcc, 0, v3
	s_cbranch_vccnz .LBB0_617
	v_readlane_b32 s4, v243, 4
	v_readlane_b32 s5, v243, 5
	s_load_dwordx2 s[8:9], s[4:5], 0x4
	s_load_dwordx4 s[40:43], s[96:97], 0xb8
	s_mov_b32 s47, 1
	v_mov_b32_e32 v17, 0
	s_waitcnt lgkmcnt(0)
	s_mul_i32 s46, s8, s33
	s_add_u32 s4, s40, 0x4200
	s_addc_u32 s5, s41, 0
	s_add_u32 s6, s40, 0x4400
	s_addc_u32 s7, s41, 0
	s_add_u32 s8, s40, 0x4500
	s_mul_i32 s46, s46, s9
	s_addc_u32 s9, s41, 0
	s_add_u32 s10, s40, 0x4600
	s_addc_u32 s11, s41, 0
	s_add_u32 s12, s40, 0x4700
	s_addc_u32 s13, s41, 0
	s_add_u32 s14, s40, 0x4800
	s_addc_u32 s15, s41, 0
	s_add_u32 s16, s40, 0x4900
	s_addc_u32 s17, s41, 0
	s_add_u32 s18, s40, 0x4a00
	s_addc_u32 s19, s41, 0
	s_add_u32 s20, s40, 0x4b00
	s_addc_u32 s21, s41, 0
	s_add_u32 s22, s40, 0x4c00
	s_addc_u32 s23, s41, 0
	s_add_u32 s24, s40, 0x4d00
	s_addc_u32 s25, s41, 0
	s_add_u32 s26, s40, 0x4e00
	s_addc_u32 s27, s41, 0
	s_add_u32 s28, s40, 0x4f00
	s_addc_u32 s29, s41, 0
	s_add_u32 s30, s40, 0x5000
	s_addc_u32 s31, s41, 0
	s_add_u32 s34, s40, 0x5100
	s_addc_u32 s35, s41, 0
	s_add_u32 s36, s40, 0x5200
	s_addc_u32 s37, s41, 0
	s_add_u32 s38, s40, 0x5300
	s_addc_u32 s39, s41, 0
	s_branch .LBB0_605

.LBB0_683:
	s_load_dwordx4 s[4:7], s[96:97], 0xb8
	s_waitcnt lgkmcnt(0)
	s_cmp_gt_i32 s7, 7
	s_cselect_b64 s[0:1], -1, 0
	s_and_b64 s[2:3], s[2:3], s[0:1]
	s_andn2_b64 vcc, exec, s[2:3]
	s_cbranch_vccnz .LBB0_737
	s_waitcnt vmcnt(0)
	s_barrier
	s_mov_b64 s[2:3], exec
	v_readlane_b32 s4, v243, 10
	v_readlane_b32 s5, v243, 11
	s_and_b64 s[4:5], s[2:3], s[4:5]
	s_mov_b64 exec, s[4:5]
	s_cbranch_execz .LBB0_736
	s_add_i32 s4, 0, 0x20000
	v_mov_b32_e32 v1, s4
	s_waitcnt vmcnt(0) expcnt(0) lgkmcnt(0)
	buffer_inv sc1
	ds_read_b32 v3, v1
	s_add_i32 s4, 0, 0x20004
	v_mov_b32_e32 v1, s4
	ds_read_b32 v1, v1
	s_waitcnt lgkmcnt(1)
	v_cmp_ne_u32_e32 vcc, 0, v3
	s_cbranch_vccnz .LBB0_700
	v_readlane_b32 s4, v243, 4
	v_readlane_b32 s5, v243, 5
	s_load_dwordx2 s[8:9], s[4:5], 0x4
	s_load_dwordx4 s[40:43], s[96:97], 0xb8
	s_mov_b32 s47, 1
	v_mov_b32_e32 v17, 0
	s_waitcnt lgkmcnt(0)
	s_mul_i32 s46, s8, s33
	s_add_u32 s4, s40, 0x4200
	s_addc_u32 s5, s41, 0
	s_add_u32 s6, s40, 0x4400
	s_addc_u32 s7, s41, 0
	s_add_u32 s8, s40, 0x4500
	s_mul_i32 s46, s46, s9
	s_addc_u32 s9, s41, 0
	s_add_u32 s10, s40, 0x4600
	s_addc_u32 s11, s41, 0
	s_add_u32 s12, s40, 0x4700
	s_addc_u32 s13, s41, 0
	s_add_u32 s14, s40, 0x4800
	s_addc_u32 s15, s41, 0
	s_add_u32 s16, s40, 0x4900
	s_addc_u32 s17, s41, 0
	s_add_u32 s18, s40, 0x4a00
	s_addc_u32 s19, s41, 0
	s_add_u32 s20, s40, 0x4b00
	s_addc_u32 s21, s41, 0
	s_add_u32 s22, s40, 0x4c00
	s_addc_u32 s23, s41, 0
	s_add_u32 s24, s40, 0x4d00
	s_addc_u32 s25, s41, 0
	s_add_u32 s26, s40, 0x4e00
	s_addc_u32 s27, s41, 0
	s_add_u32 s28, s40, 0x4f00
	s_addc_u32 s29, s41, 0
	s_add_u32 s30, s40, 0x5000
	s_addc_u32 s31, s41, 0
	s_add_u32 s34, s40, 0x5100
	s_addc_u32 s35, s41, 0
	s_add_u32 s36, s40, 0x5200
	s_addc_u32 s37, s41, 0
	s_add_u32 s38, s40, 0x5300
	s_addc_u32 s39, s41, 0
	s_branch .LBB0_688

.LBB0_764:
	s_load_dwordx4 s[4:7], s[96:97], 0xb8
	s_waitcnt lgkmcnt(0)
	s_cmp_gt_i32 s7, 8
	s_cselect_b64 s[0:1], -1, 0
	s_and_b64 s[2:3], s[2:3], s[0:1]
	s_andn2_b64 vcc, exec, s[2:3]
	s_cbranch_vccnz .LBB0_818
	s_waitcnt vmcnt(0)
	s_barrier
	s_mov_b64 s[2:3], exec
	v_readlane_b32 s4, v243, 10
	v_readlane_b32 s5, v243, 11
	s_and_b64 s[4:5], s[2:3], s[4:5]
	s_mov_b64 exec, s[4:5]
	s_cbranch_execz .LBB0_817
	s_add_i32 s4, 0, 0x20000
	v_mov_b32_e32 v1, s4
	s_waitcnt vmcnt(0) expcnt(0) lgkmcnt(0)
	buffer_inv sc1
	ds_read_b32 v3, v1
	s_add_i32 s4, 0, 0x20004
	v_mov_b32_e32 v1, s4
	ds_read_b32 v1, v1
	s_waitcnt lgkmcnt(1)
	v_cmp_ne_u32_e32 vcc, 0, v3
	s_cbranch_vccnz .LBB0_781
	v_readlane_b32 s4, v243, 4
	v_readlane_b32 s5, v243, 5
	s_load_dwordx2 s[8:9], s[4:5], 0x4
	s_load_dwordx4 s[40:43], s[96:97], 0xb8
	s_mov_b32 s47, 1
	v_mov_b32_e32 v17, 0
	s_waitcnt lgkmcnt(0)
	s_mul_i32 s46, s8, s33
	s_add_u32 s4, s40, 0x4200
	s_addc_u32 s5, s41, 0
	s_add_u32 s6, s40, 0x4400
	s_addc_u32 s7, s41, 0
	s_add_u32 s8, s40, 0x4500
	s_mul_i32 s46, s46, s9
	s_addc_u32 s9, s41, 0
	s_add_u32 s10, s40, 0x4600
	s_addc_u32 s11, s41, 0
	s_add_u32 s12, s40, 0x4700
	s_addc_u32 s13, s41, 0
	s_add_u32 s14, s40, 0x4800
	s_addc_u32 s15, s41, 0
	s_add_u32 s16, s40, 0x4900
	s_addc_u32 s17, s41, 0
	s_add_u32 s18, s40, 0x4a00
	s_addc_u32 s19, s41, 0
	s_add_u32 s20, s40, 0x4b00
	s_addc_u32 s21, s41, 0
	s_add_u32 s22, s40, 0x4c00
	s_addc_u32 s23, s41, 0
	s_add_u32 s24, s40, 0x4d00
	s_addc_u32 s25, s41, 0
	s_add_u32 s26, s40, 0x4e00
	s_addc_u32 s27, s41, 0
	s_add_u32 s28, s40, 0x4f00
	s_addc_u32 s29, s41, 0
	s_add_u32 s30, s40, 0x5000
	s_addc_u32 s31, s41, 0
	s_add_u32 s34, s40, 0x5100
	s_addc_u32 s35, s41, 0
	s_add_u32 s36, s40, 0x5200
	s_addc_u32 s37, s41, 0
	s_add_u32 s38, s40, 0x5300
	s_addc_u32 s39, s41, 0
	s_branch .LBB0_769

.LBB0_845:
	v_readlane_b32 s0, v243, 0
	v_readlane_b32 s2, v243, 2
	v_readlane_b32 s3, v243, 3
	v_readlane_b32 s1, v243, 1
	s_cmp_gt_i32 s3, 9
	v_readlane_b32 s2, v243, 20
	s_cselect_b64 s[0:1], -1, 0
	v_readlane_b32 s3, v243, 21
	s_and_b64 s[2:3], s[2:3], s[0:1]
	s_andn2_b64 vcc, exec, s[2:3]
	s_cbranch_vccnz .LBB0_899
	s_waitcnt vmcnt(0)
	s_barrier
	s_mov_b64 s[2:3], exec
	v_readlane_b32 s4, v243, 10
	v_readlane_b32 s5, v243, 11
	s_and_b64 s[4:5], s[2:3], s[4:5]
	s_mov_b64 exec, s[4:5]
	s_cbranch_execz .LBB0_898
	s_add_i32 s4, 0, 0x20000
	v_mov_b32_e32 v1, s4
	s_waitcnt vmcnt(0) expcnt(0) lgkmcnt(0)
	buffer_inv sc1
	ds_read_b32 v3, v1
	s_add_i32 s4, 0, 0x20004
	v_mov_b32_e32 v1, s4
	ds_read_b32 v1, v1
	s_waitcnt lgkmcnt(1)
	v_cmp_ne_u32_e32 vcc, 0, v3
	s_cbranch_vccnz .LBB0_862
	v_readlane_b32 s4, v243, 4
	v_readlane_b32 s5, v243, 5
	s_load_dwordx2 s[8:9], s[4:5], 0x4
	v_readlane_b32 s40, v243, 0
	v_readlane_b32 s41, v243, 1
	s_add_u32 s4, s40, 0x4200
	s_addc_u32 s5, s41, 0
	s_add_u32 s6, s40, 0x4400
	s_addc_u32 s7, s41, 0
	s_waitcnt lgkmcnt(0)
	s_mul_i32 s46, s8, s33
	s_add_u32 s8, s40, 0x4500
	s_mul_i32 s46, s46, s9
	s_addc_u32 s9, s41, 0
	s_add_u32 s10, s40, 0x4600
	s_addc_u32 s11, s41, 0
	s_add_u32 s12, s40, 0x4700
	s_addc_u32 s13, s41, 0
	s_add_u32 s14, s40, 0x4800
	s_addc_u32 s15, s41, 0
	s_add_u32 s16, s40, 0x4900
	s_addc_u32 s17, s41, 0
	s_add_u32 s18, s40, 0x4a00
	s_addc_u32 s19, s41, 0
	s_add_u32 s20, s40, 0x4b00
	s_addc_u32 s21, s41, 0
	s_add_u32 s22, s40, 0x4c00
	s_addc_u32 s23, s41, 0
	s_add_u32 s24, s40, 0x4d00
	s_addc_u32 s25, s41, 0
	s_add_u32 s26, s40, 0x4e00
	s_addc_u32 s27, s41, 0
	s_add_u32 s28, s40, 0x4f00
	s_addc_u32 s29, s41, 0
	s_add_u32 s30, s40, 0x5000
	s_addc_u32 s31, s41, 0
	s_add_u32 s34, s40, 0x5100
	s_addc_u32 s35, s41, 0
	s_add_u32 s36, s40, 0x5200
	s_addc_u32 s37, s41, 0
	s_add_u32 s38, s40, 0x5300
	s_addc_u32 s39, s41, 0
	s_mov_b32 s47, 1
	v_mov_b32_e32 v17, 0
	v_readlane_b32 s42, v243, 2
	v_readlane_b32 s43, v243, 3
	s_branch .LBB0_850

.LBB0_930:
	v_readlane_b32 s0, v243, 0
	v_readlane_b32 s3, v243, 3
	v_readlane_b32 s1, v243, 1
	s_cmp_gt_i32 s3, 10
	v_readlane_b32 s2, v243, 2
	s_cselect_b64 s[0:1], -1, 0
	s_and_b64 s[2:3], s[36:37], s[0:1]
	s_andn2_b64 vcc, exec, s[2:3]
	s_cbranch_vccnz .LBB0_984
	s_waitcnt vmcnt(0)
	s_barrier
	s_mov_b64 s[2:3], exec
	v_readlane_b32 s4, v243, 10
	v_readlane_b32 s5, v243, 11
	s_and_b64 s[4:5], s[2:3], s[4:5]
	s_mov_b64 exec, s[4:5]
	s_cbranch_execz .LBB0_983
	s_add_i32 s4, 0, 0x20000
	v_mov_b32_e32 v1, s4
	s_waitcnt vmcnt(0) expcnt(0) lgkmcnt(0)
	buffer_inv sc1
	ds_read_b32 v3, v1
	s_add_i32 s4, 0, 0x20004
	v_mov_b32_e32 v1, s4
	ds_read_b32 v1, v1
	s_waitcnt lgkmcnt(1)
	v_cmp_ne_u32_e32 vcc, 0, v3
	s_cbranch_vccnz .LBB0_947
	v_readlane_b32 s4, v243, 4
	v_readlane_b32 s5, v243, 5
	s_load_dwordx2 s[8:9], s[4:5], 0x4
	v_readlane_b32 s40, v243, 0
	v_readlane_b32 s41, v243, 1
	s_add_u32 s4, s40, 0x4200
	s_addc_u32 s5, s41, 0
	s_add_u32 s6, s40, 0x4400
	s_addc_u32 s7, s41, 0
	s_waitcnt lgkmcnt(0)
	s_mul_i32 s46, s8, s33
	s_add_u32 s8, s40, 0x4500
	s_mul_i32 s46, s46, s9
	s_addc_u32 s9, s41, 0
	s_add_u32 s10, s40, 0x4600
	s_addc_u32 s11, s41, 0
	s_add_u32 s12, s40, 0x4700
	s_addc_u32 s13, s41, 0
	s_add_u32 s14, s40, 0x4800
	s_addc_u32 s15, s41, 0
	s_add_u32 s16, s40, 0x4900
	s_addc_u32 s17, s41, 0
	s_add_u32 s18, s40, 0x4a00
	s_addc_u32 s19, s41, 0
	s_add_u32 s20, s40, 0x4b00
	s_addc_u32 s21, s41, 0
	s_add_u32 s22, s40, 0x4c00
	s_addc_u32 s23, s41, 0
	s_add_u32 s24, s40, 0x4d00
	s_addc_u32 s25, s41, 0
	s_add_u32 s26, s40, 0x4e00
	s_addc_u32 s27, s41, 0
	s_add_u32 s28, s40, 0x4f00
	s_addc_u32 s29, s41, 0
	s_add_u32 s30, s40, 0x5000
	s_addc_u32 s31, s41, 0
	s_add_u32 s34, s40, 0x5100
	s_addc_u32 s35, s41, 0
	s_add_u32 s36, s40, 0x5200
	s_addc_u32 s37, s41, 0
	s_add_u32 s38, s40, 0x5300
	s_addc_u32 s39, s41, 0
	s_mov_b32 s47, 1
	v_mov_b32_e32 v17, 0
	v_readlane_b32 s42, v243, 2
	v_readlane_b32 s43, v243, 3
	s_branch .LBB0_935

.LBB0_992:
	s_or_b64 exec, exec, s[0:1]
	v_cmp_gt_u32_e32 vcc, 64, v2
	s_waitcnt lgkmcnt(0)
	s_barrier
	s_and_saveexec_b64 s[0:1], vcc
	s_cbranch_execz .LBB0_994
	s_add_i32 s4, 0, 0x20180
	v_lshl_add_u32 v1, v2, 2, s4
	ds_read_b32 v3, v1
	ds_read_b32 v4, v1 offset:256
	s_waitcnt lgkmcnt(0)
	v_add_u32_e32 v3, 0xff, v3
	v_lshrrev_b32_e32 v3, 8, v3
	v_add_u32_e32 v4, 0xff, v4
	v_lshrrev_b32_e32 v4, 8, v4
	v_mov_b32_e32 v5, 0
	s_mov_b32 s5, 0
	s_nop 1
	v_writelane_b32 v5, s5, 0
	v_readlane_b32 s4, v3, 0
	s_nop 0
	s_add_u32 s5, s5, s4
	v_writelane_b32 v5, s5, 1
	v_readlane_b32 s4, v3, 1
	s_nop 0
	s_add_u32 s5, s5, s4
	v_writelane_b32 v5, s5, 2
	v_readlane_b32 s4, v3, 2
	s_nop 0
	s_add_u32 s5, s5, s4
	v_writelane_b32 v5, s5, 3
	v_readlane_b32 s4, v3, 3
	s_nop 0
	s_add_u32 s5, s5, s4
	v_writelane_b32 v5, s5, 4
	v_readlane_b32 s4, v3, 4
	s_nop 0
	s_add_u32 s5, s5, s4
	v_writelane_b32 v5, s5, 5
	v_readlane_b32 s4, v3, 5
	s_nop 0
	s_add_u32 s5, s5, s4
	v_writelane_b32 v5, s5, 6
	v_readlane_b32 s4, v3, 6
	s_nop 0
	s_add_u32 s5, s5, s4
	v_writelane_b32 v5, s5, 7
	v_readlane_b32 s4, v3, 7
	s_nop 0
	s_add_u32 s5, s5, s4
	v_writelane_b32 v5, s5, 8
	v_readlane_b32 s4, v3, 8
	s_nop 0
	s_add_u32 s5, s5, s4
	v_writelane_b32 v5, s5, 9
	v_readlane_b32 s4, v3, 9
	s_nop 0
	s_add_u32 s5, s5, s4
	v_writelane_b32 v5, s5, 10
	v_readlane_b32 s4, v3, 10
	s_nop 0
	s_add_u32 s5, s5, s4
	v_writelane_b32 v5, s5, 11
	v_readlane_b32 s4, v3, 11
	s_nop 0
	s_add_u32 s5, s5, s4
	v_writelane_b32 v5, s5, 12
	v_readlane_b32 s4, v3, 12
	s_nop 0
	s_add_u32 s5, s5, s4
	v_writelane_b32 v5, s5, 13
	v_readlane_b32 s4, v3, 13
	s_nop 0
	s_add_u32 s5, s5, s4
	v_writelane_b32 v5, s5, 14
	v_readlane_b32 s4, v3, 14
	s_nop 0
	s_add_u32 s5, s5, s4
	v_writelane_b32 v5, s5, 15
	v_readlane_b32 s4, v3, 15
	s_nop 0
	s_add_u32 s5, s5, s4
	v_writelane_b32 v5, s5, 16
	v_readlane_b32 s4, v3, 16
	s_nop 0
	s_add_u32 s5, s5, s4
	v_writelane_b32 v5, s5, 17
	v_readlane_b32 s4, v3, 17
	s_nop 0
	s_add_u32 s5, s5, s4
	v_writelane_b32 v5, s5, 18
	v_readlane_b32 s4, v3, 18
	s_nop 0
	s_add_u32 s5, s5, s4
	v_writelane_b32 v5, s5, 19
	v_readlane_b32 s4, v3, 19
	s_nop 0
	s_add_u32 s5, s5, s4
	v_writelane_b32 v5, s5, 20
	v_readlane_b32 s4, v3, 20
	s_nop 0
	s_add_u32 s5, s5, s4
	v_writelane_b32 v5, s5, 21
	v_readlane_b32 s4, v3, 21
	s_nop 0
	s_add_u32 s5, s5, s4
	v_writelane_b32 v5, s5, 22
	v_readlane_b32 s4, v3, 22
	s_nop 0
	s_add_u32 s5, s5, s4
	v_writelane_b32 v5, s5, 23
	v_readlane_b32 s4, v3, 23
	s_nop 0
	s_add_u32 s5, s5, s4
	v_writelane_b32 v5, s5, 24
	v_readlane_b32 s4, v3, 24
	s_nop 0
	s_add_u32 s5, s5, s4
	v_writelane_b32 v5, s5, 25
	v_readlane_b32 s4, v3, 25
	s_nop 0
	s_add_u32 s5, s5, s4
	v_writelane_b32 v5, s5, 26
	v_readlane_b32 s4, v3, 26
	s_nop 0
	s_add_u32 s5, s5, s4
	v_writelane_b32 v5, s5, 27
	v_readlane_b32 s4, v3, 27
	s_nop 0
	s_add_u32 s5, s5, s4
	v_writelane_b32 v5, s5, 28
	v_readlane_b32 s4, v3, 28
	s_nop 0
	s_add_u32 s5, s5, s4
	v_writelane_b32 v5, s5, 29
	v_readlane_b32 s4, v3, 29
	s_nop 0
	s_add_u32 s5, s5, s4
	v_writelane_b32 v5, s5, 30
	v_readlane_b32 s4, v3, 30
	s_nop 0
	s_add_u32 s5, s5, s4
	v_writelane_b32 v5, s5, 31
	v_readlane_b32 s4, v3, 31
	s_nop 0
	s_add_u32 s5, s5, s4
	v_writelane_b32 v5, s5, 32
	v_readlane_b32 s4, v3, 32
	s_nop 0
	s_add_u32 s5, s5, s4
	v_writelane_b32 v5, s5, 33
	v_readlane_b32 s4, v3, 33
	s_nop 0
	s_add_u32 s5, s5, s4
	v_writelane_b32 v5, s5, 34
	v_readlane_b32 s4, v3, 34
	s_nop 0
	s_add_u32 s5, s5, s4
	v_writelane_b32 v5, s5, 35
	v_readlane_b32 s4, v3, 35
	s_nop 0
	s_add_u32 s5, s5, s4
	v_writelane_b32 v5, s5, 36
	v_readlane_b32 s4, v3, 36
	s_nop 0
	s_add_u32 s5, s5, s4
	v_writelane_b32 v5, s5, 37
	v_readlane_b32 s4, v3, 37
	s_nop 0
	s_add_u32 s5, s5, s4
	v_writelane_b32 v5, s5, 38
	v_readlane_b32 s4, v3, 38
	s_nop 0
	s_add_u32 s5, s5, s4
	v_writelane_b32 v5, s5, 39
	v_readlane_b32 s4, v3, 39
	s_nop 0
	s_add_u32 s5, s5, s4
	v_writelane_b32 v5, s5, 40
	v_readlane_b32 s4, v3, 40
	s_nop 0
	s_add_u32 s5, s5, s4
	v_writelane_b32 v5, s5, 41
	v_readlane_b32 s4, v3, 41
	s_nop 0
	s_add_u32 s5, s5, s4
	v_writelane_b32 v5, s5, 42
	v_readlane_b32 s4, v3, 42
	s_nop 0
	s_add_u32 s5, s5, s4
	v_writelane_b32 v5, s5, 43
	v_readlane_b32 s4, v3, 43
	s_nop 0
	s_add_u32 s5, s5, s4
	v_writelane_b32 v5, s5, 44
	v_readlane_b32 s4, v3, 44
	s_nop 0
	s_add_u32 s5, s5, s4
	v_writelane_b32 v5, s5, 45
	v_readlane_b32 s4, v3, 45
	s_nop 0
	s_add_u32 s5, s5, s4
	v_writelane_b32 v5, s5, 46
	v_readlane_b32 s4, v3, 46
	s_nop 0
	s_add_u32 s5, s5, s4
	v_writelane_b32 v5, s5, 47
	v_readlane_b32 s4, v3, 47
	s_nop 0
	s_add_u32 s5, s5, s4
	v_writelane_b32 v5, s5, 48
	v_readlane_b32 s4, v3, 48
	s_nop 0
	s_add_u32 s5, s5, s4
	v_writelane_b32 v5, s5, 49
	v_readlane_b32 s4, v3, 49
	s_nop 0
	s_add_u32 s5, s5, s4
	v_writelane_b32 v5, s5, 50
	v_readlane_b32 s4, v3, 50
	s_nop 0
	s_add_u32 s5, s5, s4
	v_writelane_b32 v5, s5, 51
	v_readlane_b32 s4, v3, 51
	s_nop 0
	s_add_u32 s5, s5, s4
	v_writelane_b32 v5, s5, 52
	v_readlane_b32 s4, v3, 52
	s_nop 0
	s_add_u32 s5, s5, s4
	v_writelane_b32 v5, s5, 53
	v_readlane_b32 s4, v3, 53
	s_nop 0
	s_add_u32 s5, s5, s4
	v_writelane_b32 v5, s5, 54
	v_readlane_b32 s4, v3, 54
	s_nop 0
	s_add_u32 s5, s5, s4
	v_writelane_b32 v5, s5, 55
	v_readlane_b32 s4, v3, 55
	s_nop 0
	s_add_u32 s5, s5, s4
	v_writelane_b32 v5, s5, 56
	v_readlane_b32 s4, v3, 56
	s_nop 0
	s_add_u32 s5, s5, s4
	v_writelane_b32 v5, s5, 57
	v_readlane_b32 s4, v3, 57
	s_nop 0
	s_add_u32 s5, s5, s4
	v_writelane_b32 v5, s5, 58
	v_readlane_b32 s4, v3, 58
	s_nop 0
	s_add_u32 s5, s5, s4
	v_writelane_b32 v5, s5, 59
	v_readlane_b32 s4, v3, 59
	s_nop 0
	s_add_u32 s5, s5, s4
	v_writelane_b32 v5, s5, 60
	v_readlane_b32 s4, v3, 60
	s_nop 0
	s_add_u32 s5, s5, s4
	v_writelane_b32 v5, s5, 61
	v_readlane_b32 s4, v3, 61
	s_nop 0
	s_add_u32 s5, s5, s4
	v_writelane_b32 v5, s5, 62
	v_readlane_b32 s4, v3, 62
	s_nop 0
	s_add_u32 s5, s5, s4
	v_writelane_b32 v5, s5, 63
	v_readlane_b32 s4, v3, 63
	s_nop 0
	s_add_u32 s5, s5, s4
	v_readlane_b32 s4, v4, 0
	s_nop 0
	s_add_u32 s4, s5, s4
	s_add_i32 s6, 0, 0x20040
	v_lshl_add_u32 v1, v2, 2, s6
	ds_write_b32 v1, v5
	v_mov_b32_e32 v3, s5
	v_mov_b32_e32 v4, s4
	s_add_i32 s6, 0, 0x20140
	v_mov_b32_e32 v1, s6
	ds_write_b32 v1, v3
	ds_write_b32 v1, v4 offset:4

.LBB0_1080:
	v_readlane_b32 s4, v243, 0
	v_readlane_b32 s7, v243, 3
	s_cmp_gt_i32 s7, 11
	s_cselect_b64 s[0:1], -1, 0
	s_and_b64 s[2:3], s[2:3], s[0:1]
	s_andn2_b64 vcc, exec, s[2:3]
	v_readlane_b32 s5, v243, 1
	v_readlane_b32 s6, v243, 2
	s_cbranch_vccnz .LBB0_1134
	s_waitcnt vmcnt(0)
	s_waitcnt vmcnt(0)
	s_barrier
	s_mov_b64 s[2:3], exec
	v_readlane_b32 s4, v243, 10
	v_readlane_b32 s5, v243, 11
	s_and_b64 s[4:5], s[2:3], s[4:5]
	s_mov_b64 exec, s[4:5]
	s_cbranch_execz .LBB0_1133
	s_add_i32 s4, 0, 0x20000
	v_mov_b32_e32 v1, s4
	s_waitcnt vmcnt(0) expcnt(0) lgkmcnt(0)
	buffer_inv sc1
	ds_read_b32 v3, v1
	s_add_i32 s4, 0, 0x20004
	v_mov_b32_e32 v1, s4
	ds_read_b32 v1, v1
	s_waitcnt lgkmcnt(1)
	v_cmp_ne_u32_e32 vcc, 0, v3
	s_cbranch_vccnz .LBB0_1097
	v_readlane_b32 s4, v243, 4
	v_readlane_b32 s5, v243, 5
	s_load_dwordx2 s[8:9], s[4:5], 0x4
	v_readlane_b32 s40, v243, 0
	v_readlane_b32 s41, v243, 1
	s_add_u32 s4, s40, 0x4200
	s_addc_u32 s5, s41, 0
	s_add_u32 s6, s40, 0x4400
	s_addc_u32 s7, s41, 0
	s_waitcnt lgkmcnt(0)
	s_mul_i32 s46, s8, s33
	s_add_u32 s8, s40, 0x4500
	s_mul_i32 s46, s46, s9
	s_addc_u32 s9, s41, 0
	s_add_u32 s10, s40, 0x4600
	s_addc_u32 s11, s41, 0
	s_add_u32 s12, s40, 0x4700
	s_addc_u32 s13, s41, 0
	s_add_u32 s14, s40, 0x4800
	s_addc_u32 s15, s41, 0
	s_add_u32 s16, s40, 0x4900
	s_addc_u32 s17, s41, 0
	s_add_u32 s18, s40, 0x4a00
	s_addc_u32 s19, s41, 0
	s_add_u32 s20, s40, 0x4b00
	s_addc_u32 s21, s41, 0
	s_add_u32 s22, s40, 0x4c00
	s_addc_u32 s23, s41, 0
	s_add_u32 s24, s40, 0x4d00
	s_addc_u32 s25, s41, 0
	s_add_u32 s26, s40, 0x4e00
	s_addc_u32 s27, s41, 0
	s_add_u32 s28, s40, 0x4f00
	s_addc_u32 s29, s41, 0
	s_add_u32 s30, s40, 0x5000
	s_addc_u32 s31, s41, 0
	s_add_u32 s34, s40, 0x5100
	s_addc_u32 s35, s41, 0
	s_add_u32 s36, s40, 0x5200
	s_addc_u32 s37, s41, 0
	s_add_u32 s38, s40, 0x5300
	s_addc_u32 s39, s41, 0
	s_mov_b32 s47, 1
	v_mov_b32_e32 v17, 0
	v_readlane_b32 s42, v243, 2
	v_readlane_b32 s43, v243, 3
	s_branch .LBB0_1085

.LBB0_1149:
	v_readlane_b32 s4, v243, 0
	v_readlane_b32 s7, v243, 3
	s_cmp_gt_i32 s7, 12
	s_cselect_b64 s[2:3], -1, 0
	s_and_b64 s[0:1], s[0:1], s[2:3]
	s_andn2_b64 vcc, exec, s[0:1]
	v_readlane_b32 s5, v243, 1
	v_readlane_b32 s6, v243, 2
	s_cbranch_vccnz .LBB0_1203
	s_waitcnt vmcnt(0)
	s_waitcnt vmcnt(0)
	s_barrier
	s_mov_b64 s[0:1], exec
	v_readlane_b32 s4, v243, 10
	v_readlane_b32 s5, v243, 11
	s_and_b64 s[4:5], s[0:1], s[4:5]
	s_mov_b64 exec, s[4:5]
	s_cbranch_execz .LBB0_1202
	s_add_i32 s4, 0, 0x20000
	v_mov_b32_e32 v1, s4
	s_waitcnt vmcnt(0) expcnt(0) lgkmcnt(0)
	buffer_inv sc1
	ds_read_b32 v3, v1
	s_add_i32 s4, 0, 0x20004
	v_mov_b32_e32 v1, s4
	ds_read_b32 v1, v1
	s_waitcnt lgkmcnt(1)
	v_cmp_ne_u32_e32 vcc, 0, v3
	s_cbranch_vccnz .LBB0_1166
	v_readlane_b32 s4, v243, 4
	v_readlane_b32 s5, v243, 5
	s_load_dwordx2 s[8:9], s[4:5], 0x4
	v_readlane_b32 s40, v243, 0
	v_readlane_b32 s41, v243, 1
	s_add_u32 s4, s40, 0x4200
	s_addc_u32 s5, s41, 0
	s_add_u32 s6, s40, 0x4400
	s_addc_u32 s7, s41, 0
	s_waitcnt lgkmcnt(0)
	s_mul_i32 s33, s8, s33
	s_add_u32 s8, s40, 0x4500
	s_mul_i32 s33, s33, s9
	s_addc_u32 s9, s41, 0
	s_add_u32 s10, s40, 0x4600
	s_addc_u32 s11, s41, 0
	s_add_u32 s12, s40, 0x4700
	s_addc_u32 s13, s41, 0
	s_add_u32 s14, s40, 0x4800
	s_addc_u32 s15, s41, 0
	s_add_u32 s16, s40, 0x4900
	s_addc_u32 s17, s41, 0
	s_add_u32 s18, s40, 0x4a00
	s_addc_u32 s19, s41, 0
	s_add_u32 s20, s40, 0x4b00
	s_addc_u32 s21, s41, 0
	s_add_u32 s22, s40, 0x4c00
	s_addc_u32 s23, s41, 0
	s_add_u32 s24, s40, 0x4d00
	s_addc_u32 s25, s41, 0
	s_add_u32 s26, s40, 0x4e00
	s_addc_u32 s27, s41, 0
	s_add_u32 s28, s40, 0x4f00
	s_addc_u32 s29, s41, 0
	s_add_u32 s30, s40, 0x5000
	s_addc_u32 s31, s41, 0
	s_add_u32 s34, s40, 0x5100
	s_addc_u32 s35, s41, 0
	s_add_u32 s36, s40, 0x5200
	s_addc_u32 s37, s41, 0
	s_add_u32 s38, s40, 0x5300
	s_addc_u32 s39, s41, 0
	s_mov_b32 s46, 1
	v_mov_b32_e32 v17, 0
	v_readlane_b32 s42, v243, 2
	v_readlane_b32 s43, v243, 3
	s_branch .LBB0_1154
